# SWA unit 256-key staging: both V^T staging iterations' loads issued right behind the K loads (counted waits) instead of a load-wait round trip per iteration
# baseline (speedup 1.0000x reference)
; #define LAS __attribute__((address_space(3)))
; __device__ __forceinline__ void stage_kv(LAS unsigned char* lds, const bf16_t* kcol, const bf16_t* vcol, size_t grow0, int nk, int kc0, int tid) {
;     for (int c = tid; c < nk * 8; c += NTHR) { const int key = c >> 3, part = c & 7;
;         const u32x4 v = *(const u32x4*)(kcol + (grow0 + key) * NIN + part * 8);
;         *(LAS u32x4*)(lds + K_OFF + (kc0 + key) * KROW + part * 16) = v; }
;     const int np = nk >> 1;
;     for (int it = tid; it < np * 8; it += NTHR) { const int kp = it % np, dp = it / np;
;         const u32x4 a = *(const u32x4*)(vcol + (grow0 + 2 * kp) * NIN + dp * 8), b = *(const u32x4*)(vcol + (grow0 + 2 * kp + 1) * NIN + dp * 8);
;         LAS unsigned char* dst = lds + V_OFF + (dp * 8) * VROW + (kc0 + 2 * kp) * 2;
;         *(LAS unsigned*)(dst + 0 * VROW) = (a.x & 0xffffu) | (b.x << 16); *(LAS unsigned*)(dst + 1 * VROW) = (a.x >> 16) | (b.x & 0xffff0000u);
;         *(LAS unsigned*)(dst + 2 * VROW) = (a.y & 0xffffu) | (b.y << 16); *(LAS unsigned*)(dst + 3 * VROW) = (a.y >> 16) | (b.y & 0xffff0000u);
;         *(LAS unsigned*)(dst + 4 * VROW) = (a.z & 0xffffu) | (b.z << 16); *(LAS unsigned*)(dst + 5 * VROW) = (a.z >> 16) | (b.z & 0xffff0000u);
;         *(LAS unsigned*)(dst + 6 * VROW) = (a.w & 0xffffu) | (b.w << 16); *(LAS unsigned*)(dst + 7 * VROW) = (a.w >> 16) | (b.w & 0xffff0000u); }
; }
; __device__ __forceinline__ void swa_unit(Frame& F, const bf16_t* proj, const float* sinks, unsigned char* Y, int b, int kvh, int qb) {
;     ...
;     if (qb > 0) stage_kv(lds, kcol, vcol, rb + (size_t)qb * 128 - 128, 256, 0, F.tid);
.LBB0_895:
	v_lshl_add_u64 v[180:181], v[4:5], 0, s[42:43]
	v_lshl_add_u64 v[182:183], v[180:181], 0, s[42:43]
	v_lshl_add_u64 v[184:185], v[182:183], 0, s[42:43]
	global_load_dwordx4 v[164:167], v[4:5], off
	global_load_dwordx4 v[168:171], v[180:181], off
	global_load_dwordx4 v[172:175], v[182:183], off
	global_load_dwordx4 v[176:179], v[184:185], off
	v_lshl_add_u64 v[186:187], v[134:135], 0, s[12:13]
	v_add_co_u32_e32 v188, vcc, 0x2000, v186
	s_nop 1
	v_addc_co_u32_e32 v189, vcc, 0, v187, vcc
	global_load_dwordx4 v[8:11], v[186:187], off
	global_load_dwordx4 v[12:15], v[188:189], off offset:1536
	global_load_dwordx4 v[210:213], v[186:187], off offset:64
	global_load_dwordx4 v[214:217], v[188:189], off offset:1600
	s_waitcnt vmcnt(4)
	ds_write_b128 v6, v[164:167]
	ds_write_b128 v6, v[168:171] offset:9216
	ds_write_b128 v6, v[172:175] offset:18432
	ds_write_b128 v6, v[176:179] offset:27648
	v_lshl_add_u64 v[4:5], v[134:135], 0, s[12:13]
	s_mov_b64 s[12:13], 0
	v_mov_b32_e32 v3, v148
	v_mov_b32_e32 v6, v149
.LBB0_897:
	s_nop 0
	v_add_co_u32_e32 v3, vcc, 0x200, v3
	s_xor_b64 s[14:15], vcc, -1
	v_mad_u32_u24 v7, v6, s49, v131
	s_and_b64 s[14:15], exec, s[14:15]
	v_add_u32_e32 v6, 4, v6
	v_add_u32_e32 v16, 0x9000, v7
	v_lshl_add_u64 v[4:5], v[4:5], 0, 64
	s_or_b64 s[12:13], s[14:15], s[12:13]
	v_add_u32_e32 v17, 0x9400, v7
	v_add_u32_e32 v19, 0x9800, v7
	v_add_u32_e32 v7, 0x9c00, v7
	s_waitcnt vmcnt(3)
	v_and_b32_e32 v20, 0xffff, v8
	v_lshrrev_b32_e32 v8, 16, v8
	v_and_b32_e32 v21, 0xffff, v9
	v_lshrrev_b32_e32 v9, 16, v9
	v_and_b32_e32 v22, 0xffff, v10
	v_lshrrev_b32_e32 v10, 16, v10
	v_and_b32_e32 v23, 0xffff, v11
	v_lshrrev_b32_e32 v11, 16, v11
	s_waitcnt vmcnt(2)
	v_lshl_or_b32 v20, v12, 16, v20
	v_and_or_b32 v8, v12, s57, v8
	v_lshl_or_b32 v12, v13, 16, v21
	v_and_or_b32 v9, v13, s57, v9
	v_lshl_or_b32 v13, v14, 16, v22
	v_and_or_b32 v10, v14, s57, v10
	v_lshl_or_b32 v14, v15, 16, v23
	v_and_or_b32 v11, v15, s57, v11
	ds_write2_b32 v16, v20, v8 offset1:130
	ds_write2_b32 v17, v12, v9 offset0:4 offset1:134
	ds_write2_b32 v19, v13, v10 offset0:8 offset1:138
	ds_write2_b32 v7, v14, v11 offset0:12 offset1:142
	s_waitcnt vmcnt(0)
	v_mov_b64_e32 v[8:9], v[210:211]
	v_mov_b64_e32 v[10:11], v[212:213]
	v_mov_b64_e32 v[12:13], v[214:215]
	v_mov_b64_e32 v[14:15], v[216:217]
	s_andn2_b64 exec, exec, s[12:13]
	s_cbranch_execnz .LBB0_897
	s_or_b64 exec, exec, s[12:13]
	s_mov_b64 s[12:13], 0

; #define LAS __attribute__((address_space(3)))
; __device__ __forceinline__ void stage_kv(LAS unsigned char* lds, const bf16_t* kcol, const bf16_t* vcol, size_t grow0, int nk, int kc0, int tid) {
;     for (int c = tid; c < nk * 8; c += NTHR) { const int key = c >> 3, part = c & 7;
;         const u32x4 v = *(const u32x4*)(kcol + (grow0 + key) * NIN + part * 8);
;         *(LAS u32x4*)(lds + K_OFF + (kc0 + key) * KROW + part * 16) = v; }
;     const int np = nk >> 1;
;     for (int it = tid; it < np * 8; it += NTHR) { const int kp = it % np, dp = it / np;
;         const u32x4 a = *(const u32x4*)(vcol + (grow0 + 2 * kp) * NIN + dp * 8), b = *(const u32x4*)(vcol + (grow0 + 2 * kp + 1) * NIN + dp * 8);
;         LAS unsigned char* dst = lds + V_OFF + (dp * 8) * VROW + (kc0 + 2 * kp) * 2;
;         *(LAS unsigned*)(dst + 0 * VROW) = (a.x & 0xffffu) | (b.x << 16); *(LAS unsigned*)(dst + 1 * VROW) = (a.x >> 16) | (b.x & 0xffff0000u);
;         *(LAS unsigned*)(dst + 2 * VROW) = (a.y & 0xffffu) | (b.y << 16); *(LAS unsigned*)(dst + 3 * VROW) = (a.y >> 16) | (b.y & 0xffff0000u);
;         *(LAS unsigned*)(dst + 4 * VROW) = (a.z & 0xffffu) | (b.z << 16); *(LAS unsigned*)(dst + 5 * VROW) = (a.z >> 16) | (b.z & 0xffff0000u);
;         *(LAS unsigned*)(dst + 6 * VROW) = (a.w & 0xffffu) | (b.w << 16); *(LAS unsigned*)(dst + 7 * VROW) = (a.w >> 16) | (b.w & 0xffff0000u); }
; }
; __device__ __forceinline__ void swa_unit(Frame& F, const bf16_t* proj, const float* sinks, unsigned char* Y, int b, int kvh, int qb) {
;     ...
;     if (qb > 0) stage_kv(lds, kcol, vcol, rb + (size_t)qb * 128 - 128, 256, 0, F.tid);
.LBB0_2004:
	v_lshl_add_u64 v[180:181], v[4:5], 0, s[42:43]
	v_lshl_add_u64 v[182:183], v[180:181], 0, s[42:43]
	v_lshl_add_u64 v[184:185], v[182:183], 0, s[42:43]
	global_load_dwordx4 v[164:167], v[4:5], off
	global_load_dwordx4 v[168:171], v[180:181], off
	global_load_dwordx4 v[172:175], v[182:183], off
	global_load_dwordx4 v[176:179], v[184:185], off
	v_lshl_add_u64 v[186:187], v[134:135], 0, s[12:13]
	v_add_co_u32_e32 v188, vcc, 0x2000, v186
	s_nop 1
	v_addc_co_u32_e32 v189, vcc, 0, v187, vcc
	global_load_dwordx4 v[8:11], v[186:187], off
	global_load_dwordx4 v[12:15], v[188:189], off offset:1536
	global_load_dwordx4 v[210:213], v[186:187], off offset:64
	global_load_dwordx4 v[214:217], v[188:189], off offset:1600
	s_waitcnt vmcnt(4)
	ds_write_b128 v7, v[164:167]
	ds_write_b128 v7, v[168:171] offset:9216
	ds_write_b128 v7, v[172:175] offset:18432
	ds_write_b128 v7, v[176:179] offset:27648
	v_lshl_add_u64 v[4:5], v[134:135], 0, s[12:13]
	s_mov_b64 s[12:13], 0
	v_mov_b32_e32 v6, v143
	v_mov_b32_e32 v7, v148
.LBB0_2006:
	s_nop 0
	v_add_co_u32_e32 v6, vcc, 0x200, v6
	s_xor_b64 s[14:15], vcc, -1
	v_mad_u32_u24 v16, v7, s49, v1
	s_and_b64 s[14:15], exec, s[14:15]
	v_add_u32_e32 v7, 4, v7
	v_add_u32_e32 v17, 0x9000, v16
	v_lshl_add_u64 v[4:5], v[4:5], 0, 64
	s_or_b64 s[12:13], s[14:15], s[12:13]
	v_add_u32_e32 v19, 0x9400, v16
	v_add_u32_e32 v20, 0x9800, v16
	v_add_u32_e32 v16, 0x9c00, v16
	s_waitcnt vmcnt(3)
	v_and_b32_e32 v21, 0xffff, v8
	v_lshrrev_b32_e32 v8, 16, v8
	v_and_b32_e32 v22, 0xffff, v9
	v_lshrrev_b32_e32 v9, 16, v9
	v_and_b32_e32 v23, 0xffff, v10
	v_lshrrev_b32_e32 v10, 16, v10
	v_and_b32_e32 v24, 0xffff, v11
	v_lshrrev_b32_e32 v11, 16, v11
	s_waitcnt vmcnt(2)
	v_lshl_or_b32 v21, v12, 16, v21
	v_and_or_b32 v8, v12, s65, v8
	v_lshl_or_b32 v12, v13, 16, v22
	v_and_or_b32 v9, v13, s65, v9
	v_lshl_or_b32 v13, v14, 16, v23
	v_and_or_b32 v10, v14, s65, v10
	v_lshl_or_b32 v14, v15, 16, v24
	v_and_or_b32 v11, v15, s65, v11
	ds_write2_b32 v17, v21, v8 offset1:130
	ds_write2_b32 v19, v12, v9 offset0:4 offset1:134
	ds_write2_b32 v20, v13, v10 offset0:8 offset1:138
	ds_write2_b32 v16, v14, v11 offset0:12 offset1:142
	s_waitcnt vmcnt(0)
	v_mov_b64_e32 v[8:9], v[210:211]
	v_mov_b64_e32 v[10:11], v[212:213]
	v_mov_b64_e32 v[12:13], v[214:215]
	v_mov_b64_e32 v[14:15], v[216:217]
	s_andn2_b64 exec, exec, s[12:13]
	s_cbranch_execnz .LBB0_2006
	s_or_b64 exec, exec, s[12:13]
	s_mov_b64 s[12:13], 0
